# speedup vs baseline: 1.0273x; 1.0023x over previous
_Z6k_gramILi0EEvPK15HIP_vector_typeIjLj4EEPyPf:
	s_load_dwordx4 s[8:11], s[0:1], 0x0
	s_load_dwordx2 s[4:5], s[0:1], 0x10
	s_lshl_b32 s0, s2, 2
	s_and_b32 s0, s0, 28
	s_ashr_i32 s1, s2, 6
	s_add_i32 s16, s0, s1
	v_readfirstlane_b32 s23, v0
	s_ashr_i32 s17, s16, 31
	s_lshr_b32 s21, s23, 6
	s_bfe_u32 s18, s23, 0x20006
	s_lshr_b32 s22, s2, 3
	s_bfe_u32 s20, s2, 0x30003
	s_lshl_b64 s[0:1], s[16:17], 20
	s_waitcnt lgkmcnt(0)
	s_add_u32 s12, s8, s0
	v_mov_b32_e32 v1, 0x20000
	s_addc_u32 s0, s9, s1
	s_lshl_b32 s1, s20, 2
	v_lshl_or_b32 v1, v0, 2, v1
	v_bfrev_b32_e32 v2, 1
	s_cmp_lt_u32 s20, 4
	ds_write_b32 v1, v2
	s_mov_b32 s24, 4
	s_mov_b32 s15, 0x20000
	s_and_b32 s13, s0, 0xffff
	s_mov_b32 s14, 0x100000
	v_lshlrev_b32_e32 v166, 4, v0
	s_lshl_b32 s25, s21, 10
	s_lshl_b32 s0, s20, 17
	s_mov_b32 m0, s25
	s_nop 0
	buffer_load_dwordx4 v166, s[12:15], s0 offen lds
	s_add_i32 s26, s25, 0x2000
	s_or_b32 s2, s0, 0x2000
	s_mov_b32 m0, s26
	s_nop 0
	buffer_load_dwordx4 v166, s[12:15], s2 offen lds
	s_add_i32 s27, s25, 0x4000
	s_or_b32 s2, s0, 0x8000
	s_mov_b32 m0, s27
	s_nop 0
	buffer_load_dwordx4 v166, s[12:15], s2 offen lds
	s_add_i32 s28, s25, 0x6000
	s_or_b32 s2, s0, 0xa000
	s_mov_b32 m0, s28
	s_nop 0
	buffer_load_dwordx4 v166, s[12:15], s2 offen lds
	s_add_i32 s34, s25, 0x10000
	s_or_b32 s2, s0, 0x10000
	s_mov_b32 m0, s34
	s_nop 0
	buffer_load_dwordx4 v166, s[12:15], s2 offen lds
	s_add_i32 s35, s25, 0x12000
	s_or_b32 s2, s0, 0x12000
	s_mov_b32 m0, s35
	s_nop 0
	buffer_load_dwordx4 v166, s[12:15], s2 offen lds
	s_add_i32 s36, s25, 0x14000
	s_or_b32 s2, s0, 0x18000
	s_mov_b32 m0, s36
	s_nop 0
	buffer_load_dwordx4 v166, s[12:15], s2 offen lds
	s_add_i32 s37, s25, 0x16000
	s_or_b32 s2, s0, 0x1a000
	s_mov_b32 m0, s37
	s_nop 0
	buffer_load_dwordx4 v166, s[12:15], s2 offen lds
	s_add_i32 s29, s25, 0x8000
	s_or_b32 s2, s0, 0x4000
	s_mov_b32 m0, s29
	s_nop 0
	buffer_load_dwordx4 v166, s[12:15], s2 offen lds
	s_add_i32 s30, s25, 0xa000
	s_or_b32 s2, s0, 0x6000
	s_mov_b32 m0, s30
	s_nop 0
	buffer_load_dwordx4 v166, s[12:15], s2 offen lds
	s_add_i32 s31, s25, 0xc000
	s_or_b32 s2, s0, 0xc000
	s_mov_b32 m0, s31
	s_nop 0
	buffer_load_dwordx4 v166, s[12:15], s2 offen lds
	s_add_i32 s33, s25, 0xe000
	s_or_b32 s2, s0, 0xe000
	s_mov_b32 m0, s33
	s_nop 0
	buffer_load_dwordx4 v166, s[12:15], s2 offen lds
	s_add_i32 s38, s25, 0x18000
	s_or_b32 s2, s0, 0x14000
	s_mov_b32 m0, s38
	s_nop 0
	buffer_load_dwordx4 v166, s[12:15], s2 offen lds
	s_add_i32 s39, s25, 0x1a000
	s_or_b32 s2, s0, 0x16000
	s_mov_b32 m0, s39
	s_nop 0
	buffer_load_dwordx4 v166, s[12:15], s2 offen lds
	s_add_i32 s40, s25, 0x1c000
	s_or_b32 s2, s0, 0x1c000
	s_mov_b32 m0, s40
	s_nop 0
	buffer_load_dwordx4 v166, s[12:15], s2 offen lds
	s_add_i32 s42, s25, 0x1e000
	s_or_b32 s2, s0, 0x1e000
	s_mov_b32 m0, s42
	s_nop 0
	buffer_load_dwordx4 v166, s[12:15], s2 offen lds
	s_lshl_b32 s0, s23, 9
	s_lshl_b32 s2, s23, 8
	v_and_b32_e32 v167, 15, v0
	v_bfe_u32 v160, v0, 4, 2
	s_and_b32 s0, s0, 0x10000
	s_and_b32 s2, s2, 0x4000
	v_lshlrev_b32_e32 v128, 9, v160
	v_lshlrev_b32_e32 v129, 4, v167
	s_or_b32 s0, s0, s2
	v_or3_b32 v124, s0, v128, v129
	s_waitcnt vmcnt(8)
	s_waitcnt lgkmcnt(0)
	s_barrier
	ds_read_b128 v[0:3], v124
	ds_read_b128 v[4:7], v124 offset:256
	ds_read_b128 v[8:11], v124 offset:2048
	ds_read_b128 v[12:15], v124 offset:2304
	ds_read_b128 v[16:19], v124 offset:4096
	ds_read_b128 v[20:23], v124 offset:4352
	ds_read_b128 v[24:27], v124 offset:6144
	ds_read_b128 v[28:31], v124 offset:6400
	ds_read_b128 v[32:35], v124 offset:8192
	ds_read_b128 v[36:39], v124 offset:8448
	ds_read_b128 v[40:43], v124 offset:10240
	ds_read_b128 v[44:47], v124 offset:10496
	ds_read_b128 v[48:51], v124 offset:12288
	ds_read_b128 v[52:55], v124 offset:12544
	ds_read_b128 v[56:59], v124 offset:14336
	ds_read_b128 v[60:63], v124 offset:14592
	s_lshr_b32 s41, s23, 8
	s_lshl_b32 s0, s41, 14
	s_lshl_b32 s50, s24, 2
	v_or3_b32 v168, s0, v128, v129
	s_or_b32 s43, s18, s1
	s_lshl_b32 s0, s16, 10
	s_lshl_b32 s1, s43, 5
	ds_read_b128 v[128:131], v168
	ds_read_b128 v[132:135], v168 offset:256
	ds_read_b128 v[136:139], v168 offset:2048
	ds_read_b128 v[140:143], v168 offset:2304
	s_or_b32 s0, s1, s0
	v_or_b32_e32 v144, s0, v167
	v_lshlrev_b32_e32 v146, 2, v160
	v_ashrrev_i32_e32 v145, 31, v144
	v_lshl_add_u64 v[164:165], v[144:145], 2, s[4:5]
	v_or_b32_e32 v144, 1, v146
	v_cmp_eq_u32_e64 s[2:3], v144, v167
	v_or_b32_e32 v144, 2, v146
	s_waitcnt vmcnt(8)
	v_cmp_eq_u32_e64 s[4:5], v144, v167
	v_or_b32_e32 v144, 3, v146
	s_add_i32 s44, s50, 3
	s_lshl_b32 s45, s22, 2
	v_cmp_eq_u32_e64 s[0:1], v146, v167
	v_cmp_eq_u32_e64 s[6:7], v144, v167
	v_add_u32_e32 v169, 0x10000, v168
	v_add_u32_e32 v170, 0x10100, v168
	v_add_u32_e32 v171, 0x10800, v168
	v_add_u32_e32 v172, 0x10900, v168
	s_barrier
	s_and_b32 s8, s45, 28
	s_add_i32 s8, s8, s41
	s_lshl_b32 s19, s8, 1
	s_or_b32 s51, s19, 1
	v_mov_b32_e32 v234, s19
	v_mov_b32_e32 v235, s51
	s_and_b32 s46, s21, 3
	s_lshl_b32 s46, s46, 5
	v_lshl_or_b32 v173, v160, 3, s46
	s_lshl_b32 s47, s41, 7
	s_mov_b32 s48, 0
	s_movk_i32 s49, 0xffc0
	v_add_u32_e32 v174, 0x11000, v168
	v_add_u32_e32 v175, 0x11100, v168
	v_add_u32_e32 v176, 0x11800, v168
	v_add_u32_e32 v177, 0x11900, v168
	v_add_u32_e32 v178, 0x12000, v168
	v_add_u32_e32 v179, 0x12100, v168
	v_add_u32_e32 v180, 0x12800, v168
	v_add_u32_e32 v181, 0x12900, v168
	v_add_u32_e32 v182, 0x13000, v168
	v_add_u32_e32 v183, 0x13100, v168
	v_add_u32_e32 v184, 0x13800, v168
	v_add_u32_e32 v185, 0x13900, v168
	v_add_u32_e32 v186, 0x18000, v168
	v_add_u32_e32 v187, 0x18100, v168
	v_add_u32_e32 v188, 0x18800, v168
	v_add_u32_e32 v189, 0x18900, v168
	v_add_u32_e32 v190, 0x19000, v168
	v_add_u32_e32 v191, 0x19100, v168
	v_add_u32_e32 v192, 0x19800, v168
	v_add_u32_e32 v193, 0x19900, v168
	v_add_u32_e32 v194, 0x1a000, v168
	v_add_u32_e32 v195, 0x1a100, v168
	v_add_u32_e32 v196, 0x1a800, v168
	v_add_u32_e32 v197, 0x1a900, v168
	v_add_u32_e32 v198, 0x1b000, v168
	v_add_u32_e32 v199, 0x1b100, v168
	v_add_u32_e32 v200, 0x1b800, v168
	v_add_u32_e32 v201, 0x1b900, v168
	ds_read_b128 v[144:147], v168 offset:0
	ds_read_b128 v[148:151], v168 offset:256
	ds_read_b128 v[152:155], v168 offset:2048
	ds_read_b128 v[156:159], v168 offset:2304
	ds_read_b128 v[224:227], v168 offset:4096
	s_waitcnt lgkmcnt(4)
	v_mfma_f32_16x16x32_bf16 v[208:211], v[0:3], v[144:147], 0
	v_mfma_f32_16x16x32_bf16 v[212:215], v[4:7], v[144:147], 0
	ds_read_b128 v[228:231], v168 offset:4352
	s_waitcnt lgkmcnt(4)
	v_mfma_f32_16x16x32_bf16 v[216:219], v[0:3], v[148:151], 0
	v_mfma_f32_16x16x32_bf16 v[220:223], v[4:7], v[148:151], 0
	ds_read_b128 v[144:147], v168 offset:6144
	s_waitcnt lgkmcnt(4)
	v_mfma_f32_16x16x32_bf16 v[208:211], v[8:11], v[152:155], v[208:211]
	v_mfma_f32_16x16x32_bf16 v[212:215], v[12:15], v[152:155], v[212:215]
	ds_read_b128 v[148:151], v168 offset:6400
	s_waitcnt lgkmcnt(4)
	v_mfma_f32_16x16x32_bf16 v[216:219], v[8:11], v[156:159], v[216:219]
	v_mfma_f32_16x16x32_bf16 v[220:223], v[12:15], v[156:159], v[220:223]
	ds_read_b128 v[152:155], v168 offset:8192
	s_waitcnt lgkmcnt(4)
	v_mfma_f32_16x16x32_bf16 v[208:211], v[16:19], v[224:227], v[208:211]
	v_mfma_f32_16x16x32_bf16 v[212:215], v[20:23], v[224:227], v[212:215]
	ds_read_b128 v[156:159], v168 offset:8448
	s_waitcnt lgkmcnt(4)
	v_mfma_f32_16x16x32_bf16 v[216:219], v[16:19], v[228:231], v[216:219]
	v_mfma_f32_16x16x32_bf16 v[220:223], v[20:23], v[228:231], v[220:223]
	ds_read_b128 v[224:227], v168 offset:10240
	s_waitcnt lgkmcnt(4)
	v_mfma_f32_16x16x32_bf16 v[208:211], v[24:27], v[144:147], v[208:211]
	v_mfma_f32_16x16x32_bf16 v[212:215], v[28:31], v[144:147], v[212:215]
	ds_read_b128 v[228:231], v168 offset:10496
	s_waitcnt lgkmcnt(4)
	v_mfma_f32_16x16x32_bf16 v[216:219], v[24:27], v[148:151], v[216:219]
	v_mfma_f32_16x16x32_bf16 v[220:223], v[28:31], v[148:151], v[220:223]
	ds_read_b128 v[144:147], v168 offset:12288
	s_waitcnt lgkmcnt(4)
	v_mfma_f32_16x16x32_bf16 v[208:211], v[32:35], v[152:155], v[208:211]
	v_mfma_f32_16x16x32_bf16 v[212:215], v[36:39], v[152:155], v[212:215]
	ds_read_b128 v[148:151], v168 offset:12544
	s_waitcnt lgkmcnt(4)
	v_mfma_f32_16x16x32_bf16 v[216:219], v[32:35], v[156:159], v[216:219]
	v_mfma_f32_16x16x32_bf16 v[220:223], v[36:39], v[156:159], v[220:223]
	ds_read_b128 v[152:155], v168 offset:14336
	s_waitcnt lgkmcnt(4)
	v_mfma_f32_16x16x32_bf16 v[208:211], v[40:43], v[224:227], v[208:211]
	v_mfma_f32_16x16x32_bf16 v[212:215], v[44:47], v[224:227], v[212:215]
	ds_read_b128 v[156:159], v168 offset:14592
	s_waitcnt lgkmcnt(4)
	v_mfma_f32_16x16x32_bf16 v[216:219], v[40:43], v[228:231], v[216:219]
	v_mfma_f32_16x16x32_bf16 v[220:223], v[44:47], v[228:231], v[220:223]
	s_waitcnt lgkmcnt(3)
	v_mfma_f32_16x16x32_bf16 v[208:211], v[48:51], v[144:147], v[208:211]
	v_mfma_f32_16x16x32_bf16 v[212:215], v[52:55], v[144:147], v[212:215]
	s_waitcnt lgkmcnt(2)
	v_mfma_f32_16x16x32_bf16 v[216:219], v[48:51], v[148:151], v[216:219]
	v_mfma_f32_16x16x32_bf16 v[220:223], v[52:55], v[148:151], v[220:223]
	s_waitcnt lgkmcnt(1)
	v_mfma_f32_16x16x32_bf16 v[208:211], v[56:59], v[152:155], v[208:211]
	v_mfma_f32_16x16x32_bf16 v[212:215], v[60:63], v[152:155], v[212:215]
	s_waitcnt lgkmcnt(0)
	v_mfma_f32_16x16x32_bf16 v[216:219], v[56:59], v[156:159], v[216:219]
	v_mfma_f32_16x16x32_bf16 v[220:223], v[60:63], v[156:159], v[220:223]
	s_barrier
	s_add_i32 s60, s45, 4
	s_and_b32 s60, s60, 28
	s_lshl_b32 s60, s60, 15
	ds_read_b128 v[144:147], v169 offset:0
	ds_read_b128 v[148:151], v169 offset:256
	ds_read_b128 v[152:155], v169 offset:2048
	ds_read_b128 v[156:159], v169 offset:2304
	ds_read_b128 v[224:227], v169 offset:4096
	s_waitcnt lgkmcnt(4)
	v_mfma_f32_16x16x32_bf16 v[136:139], v[0:3], v[144:147], 0
	v_mfma_f32_16x16x32_bf16 v[128:131], v[4:7], v[144:147], 0
	ds_read_b128 v[228:231], v169 offset:4352
	s_waitcnt lgkmcnt(4)
	v_mfma_f32_16x16x32_bf16 v[140:143], v[0:3], v[148:151], 0
	s_mov_b32 s61, s60
	s_mov_b32 m0, s25
	s_nop 0
	buffer_load_dwordx4 v166, s[12:15], s61 offen lds
	v_mfma_f32_16x16x32_bf16 v[132:135], v[4:7], v[148:151], 0
	ds_read_b128 v[144:147], v169 offset:6144
	s_waitcnt lgkmcnt(4)
	v_mfma_f32_16x16x32_bf16 v[136:139], v[8:11], v[152:155], v[136:139]
	v_mfma_f32_16x16x32_bf16 v[128:131], v[12:15], v[152:155], v[128:131]
	ds_read_b128 v[148:151], v169 offset:6400
	s_waitcnt lgkmcnt(4)
	v_mfma_f32_16x16x32_bf16 v[140:143], v[8:11], v[156:159], v[140:143]
	v_mfma_f32_16x16x32_bf16 v[132:135], v[12:15], v[156:159], v[132:135]
	ds_read_b128 v[152:155], v169 offset:8192
	s_waitcnt lgkmcnt(4)
	v_mfma_f32_16x16x32_bf16 v[136:139], v[16:19], v[224:227], v[136:139]
	v_mfma_f32_16x16x32_bf16 v[128:131], v[20:23], v[224:227], v[128:131]
	ds_read_b128 v[156:159], v169 offset:8448
	s_waitcnt lgkmcnt(4)
	v_mfma_f32_16x16x32_bf16 v[140:143], v[16:19], v[228:231], v[140:143]
	s_or_b32 s61, s60, 0x2000
	s_mov_b32 m0, s26
	s_nop 0
	buffer_load_dwordx4 v166, s[12:15], s61 offen lds
	v_mfma_f32_16x16x32_bf16 v[132:135], v[20:23], v[228:231], v[132:135]
	ds_read_b128 v[224:227], v169 offset:10240
	s_waitcnt lgkmcnt(4)
	v_mfma_f32_16x16x32_bf16 v[136:139], v[24:27], v[144:147], v[136:139]
	v_mfma_f32_16x16x32_bf16 v[128:131], v[28:31], v[144:147], v[128:131]
	ds_read_b128 v[228:231], v169 offset:10496
	s_waitcnt lgkmcnt(4)
	v_mfma_f32_16x16x32_bf16 v[140:143], v[24:27], v[148:151], v[140:143]
	v_mfma_f32_16x16x32_bf16 v[132:135], v[28:31], v[148:151], v[132:135]
	ds_read_b128 v[144:147], v169 offset:12288
	s_waitcnt lgkmcnt(4)
	v_mfma_f32_16x16x32_bf16 v[136:139], v[32:35], v[152:155], v[136:139]
	v_mfma_f32_16x16x32_bf16 v[128:131], v[36:39], v[152:155], v[128:131]
	ds_read_b128 v[148:151], v169 offset:12544
	s_waitcnt lgkmcnt(4)
	v_mfma_f32_16x16x32_bf16 v[140:143], v[32:35], v[156:159], v[140:143]
	s_or_b32 s61, s60, 0x8000
	s_mov_b32 m0, s27
	s_nop 0
	buffer_load_dwordx4 v166, s[12:15], s61 offen lds
	v_mfma_f32_16x16x32_bf16 v[132:135], v[36:39], v[156:159], v[132:135]
	ds_read_b128 v[152:155], v169 offset:14336
	s_waitcnt lgkmcnt(4)
	v_mfma_f32_16x16x32_bf16 v[136:139], v[40:43], v[224:227], v[136:139]
	v_mfma_f32_16x16x32_bf16 v[128:131], v[44:47], v[224:227], v[128:131]
	ds_read_b128 v[156:159], v169 offset:14592
	s_waitcnt lgkmcnt(4)
	v_mfma_f32_16x16x32_bf16 v[140:143], v[40:43], v[228:231], v[140:143]
	v_mfma_f32_16x16x32_bf16 v[132:135], v[44:47], v[228:231], v[132:135]
	s_waitcnt lgkmcnt(3)
	v_mfma_f32_16x16x32_bf16 v[136:139], v[48:51], v[144:147], v[136:139]
	v_mfma_f32_16x16x32_bf16 v[128:131], v[52:55], v[144:147], v[128:131]
	s_waitcnt lgkmcnt(2)
	v_mfma_f32_16x16x32_bf16 v[140:143], v[48:51], v[148:151], v[140:143]
	s_or_b32 s61, s60, 0xa000
	s_mov_b32 m0, s28
	s_nop 0
	buffer_load_dwordx4 v166, s[12:15], s61 offen lds
	v_mfma_f32_16x16x32_bf16 v[132:135], v[52:55], v[148:151], v[132:135]
	s_waitcnt lgkmcnt(1)
	v_mfma_f32_16x16x32_bf16 v[136:139], v[56:59], v[152:155], v[136:139]
	v_mfma_f32_16x16x32_bf16 v[128:131], v[60:63], v[152:155], v[128:131]
	s_waitcnt lgkmcnt(0)
	v_mfma_f32_16x16x32_bf16 v[140:143], v[56:59], v[156:159], v[140:143]
	v_mfma_f32_16x16x32_bf16 v[132:135], v[60:63], v[156:159], v[132:135]
	s_waitcnt vmcnt(4)
	s_barrier
	ds_read_b128 v[64:67], v124 offset:32768
	ds_read_b128 v[68:71], v124 offset:33024
	ds_read_b128 v[72:75], v124 offset:34816
	ds_read_b128 v[76:79], v124 offset:35072
	ds_read_b128 v[80:83], v124 offset:36864
	ds_read_b128 v[84:87], v124 offset:37120
	ds_read_b128 v[88:91], v124 offset:38912
	ds_read_b128 v[92:95], v124 offset:39168
	ds_read_b128 v[96:99], v124 offset:40960
	ds_read_b128 v[100:103], v124 offset:41216
	ds_read_b128 v[104:107], v124 offset:43008
	ds_read_b128 v[108:111], v124 offset:43264
	ds_read_b128 v[112:115], v124 offset:45056
	ds_read_b128 v[116:119], v124 offset:45312
	ds_read_b128 v[120:123], v124 offset:47104
	ds_read_b128 v[124:127], v124 offset:47360
	s_add_i32 s60, s45, 4
	s_and_b32 s60, s60, 28
	s_or_b32 s60, s60, 2
	s_lshl_b32 s60, s60, 15
	ds_read_b128 v[144:147], v168 offset:32768
	ds_read_b128 v[148:151], v168 offset:33024
	ds_read_b128 v[152:155], v168 offset:34816
	ds_read_b128 v[156:159], v168 offset:35072
	ds_read_b128 v[224:227], v168 offset:36864
	s_waitcnt lgkmcnt(4)
	v_mfma_f32_16x16x32_bf16 v[208:211], v[64:67], v[144:147], v[208:211]
	v_mfma_f32_16x16x32_bf16 v[212:215], v[68:71], v[144:147], v[212:215]
	ds_read_b128 v[228:231], v168 offset:37120
	s_waitcnt lgkmcnt(4)
	v_mfma_f32_16x16x32_bf16 v[216:219], v[64:67], v[148:151], v[216:219]
	s_mov_b32 s61, s60
	s_mov_b32 m0, s34
	s_nop 0
	buffer_load_dwordx4 v166, s[12:15], s61 offen lds
	v_mfma_f32_16x16x32_bf16 v[220:223], v[68:71], v[148:151], v[220:223]
	ds_read_b128 v[144:147], v168 offset:38912
	s_waitcnt lgkmcnt(4)
	v_mfma_f32_16x16x32_bf16 v[208:211], v[72:75], v[152:155], v[208:211]
	v_mfma_f32_16x16x32_bf16 v[212:215], v[76:79], v[152:155], v[212:215]
	ds_read_b128 v[148:151], v168 offset:39168
	s_waitcnt lgkmcnt(4)
	v_mfma_f32_16x16x32_bf16 v[216:219], v[72:75], v[156:159], v[216:219]
	v_mfma_f32_16x16x32_bf16 v[220:223], v[76:79], v[156:159], v[220:223]
	ds_read_b128 v[152:155], v168 offset:40960
	s_waitcnt lgkmcnt(4)
	v_mfma_f32_16x16x32_bf16 v[208:211], v[80:83], v[224:227], v[208:211]
	v_mfma_f32_16x16x32_bf16 v[212:215], v[84:87], v[224:227], v[212:215]
	ds_read_b128 v[156:159], v168 offset:41216
	s_waitcnt lgkmcnt(4)
	v_mfma_f32_16x16x32_bf16 v[216:219], v[80:83], v[228:231], v[216:219]
	s_or_b32 s61, s60, 0x2000
	s_mov_b32 m0, s35
	s_nop 0
	buffer_load_dwordx4 v166, s[12:15], s61 offen lds
	v_mfma_f32_16x16x32_bf16 v[220:223], v[84:87], v[228:231], v[220:223]
	ds_read_b128 v[224:227], v168 offset:43008
	s_waitcnt lgkmcnt(4)
	v_mfma_f32_16x16x32_bf16 v[208:211], v[88:91], v[144:147], v[208:211]
	v_mfma_f32_16x16x32_bf16 v[212:215], v[92:95], v[144:147], v[212:215]
	ds_read_b128 v[228:231], v168 offset:43264
	s_waitcnt lgkmcnt(4)
	v_mfma_f32_16x16x32_bf16 v[216:219], v[88:91], v[148:151], v[216:219]
	v_mfma_f32_16x16x32_bf16 v[220:223], v[92:95], v[148:151], v[220:223]
	ds_read_b128 v[144:147], v168 offset:45056
	s_waitcnt lgkmcnt(4)
	v_mfma_f32_16x16x32_bf16 v[208:211], v[96:99], v[152:155], v[208:211]
	v_mfma_f32_16x16x32_bf16 v[212:215], v[100:103], v[152:155], v[212:215]
	ds_read_b128 v[148:151], v168 offset:45312
	s_waitcnt lgkmcnt(4)
	v_mfma_f32_16x16x32_bf16 v[216:219], v[96:99], v[156:159], v[216:219]
	s_or_b32 s61, s60, 0x8000
	s_mov_b32 m0, s36
	s_nop 0
	buffer_load_dwordx4 v166, s[12:15], s61 offen lds
	v_mfma_f32_16x16x32_bf16 v[220:223], v[100:103], v[156:159], v[220:223]
	ds_read_b128 v[152:155], v168 offset:47104
	s_waitcnt lgkmcnt(4)
	v_mfma_f32_16x16x32_bf16 v[208:211], v[104:107], v[224:227], v[208:211]
	v_mfma_f32_16x16x32_bf16 v[212:215], v[108:111], v[224:227], v[212:215]
	ds_read_b128 v[156:159], v168 offset:47360
	s_waitcnt lgkmcnt(4)
	v_mfma_f32_16x16x32_bf16 v[216:219], v[104:107], v[228:231], v[216:219]
	v_mfma_f32_16x16x32_bf16 v[220:223], v[108:111], v[228:231], v[220:223]
	s_waitcnt lgkmcnt(3)
	v_mfma_f32_16x16x32_bf16 v[208:211], v[112:115], v[144:147], v[208:211]
	v_mfma_f32_16x16x32_bf16 v[212:215], v[116:119], v[144:147], v[212:215]
	s_waitcnt lgkmcnt(2)
	v_mfma_f32_16x16x32_bf16 v[216:219], v[112:115], v[148:151], v[216:219]
	s_or_b32 s61, s60, 0xa000
	s_mov_b32 m0, s37
	s_nop 0
	buffer_load_dwordx4 v166, s[12:15], s61 offen lds
	v_mfma_f32_16x16x32_bf16 v[220:223], v[116:119], v[148:151], v[220:223]
	s_waitcnt lgkmcnt(1)
	v_mfma_f32_16x16x32_bf16 v[208:211], v[120:123], v[152:155], v[208:211]
	v_mfma_f32_16x16x32_bf16 v[212:215], v[124:127], v[152:155], v[212:215]
	s_waitcnt lgkmcnt(0)
	v_mfma_f32_16x16x32_bf16 v[216:219], v[120:123], v[156:159], v[216:219]
	v_mfma_f32_16x16x32_bf16 v[220:223], v[124:127], v[156:159], v[220:223]
	s_waitcnt vmcnt(4)
	s_barrier
	s_nop 7
	s_nop 3
	s_cmp_lg_u32 s8, s43
	s_cbranch_scc1 .Ldiag0_done
	s_mov_b64 s[56:57], exec
	s_and_b64 exec, s[56:57], s[0:1]
	global_store_dword v[164:165], v208, off
	v_mov_b32_e32 v208, -1.0
	global_store_dword v[164:165], v220, off offset:64
	v_mov_b32_e32 v220, -1.0
	s_and_b64 exec, s[56:57], s[2:3]
	global_store_dword v[164:165], v209, off
	v_mov_b32_e32 v209, -1.0
	global_store_dword v[164:165], v221, off offset:64
	v_mov_b32_e32 v221, -1.0
	s_and_b64 exec, s[56:57], s[4:5]
	global_store_dword v[164:165], v210, off
	v_mov_b32_e32 v210, -1.0
	global_store_dword v[164:165], v222, off offset:64
	v_mov_b32_e32 v222, -1.0
	s_and_b64 exec, s[56:57], s[6:7]
	global_store_dword v[164:165], v211, off
	v_mov_b32_e32 v211, -1.0
	global_store_dword v[164:165], v223, off offset:64
	v_mov_b32_e32 v223, -1.0
	s_mov_b64 exec, s[56:57]
.Ldiag0_done:
	s_add_i32 s60, s45, 4
	s_and_b32 s60, s60, 28
	s_lshl_b32 s60, s60, 15
	ds_read_b128 v[144:147], v169 offset:32768
	ds_read_b128 v[148:151], v169 offset:33024
	ds_read_b128 v[152:155], v169 offset:34816
	ds_read_b128 v[156:159], v169 offset:35072
	ds_read_b128 v[224:227], v169 offset:36864
	s_waitcnt lgkmcnt(4)
	v_mfma_f32_16x16x32_bf16 v[136:139], v[64:67], v[144:147], v[136:139]
	v_mfma_f32_16x16x32_bf16 v[128:131], v[68:71], v[144:147], v[128:131]
	ds_read_b128 v[228:231], v169 offset:37120
	s_waitcnt lgkmcnt(4)
	v_mfma_f32_16x16x32_bf16 v[140:143], v[64:67], v[148:151], v[140:143]
	s_or_b32 s61, s60, 0x4000
	s_mov_b32 m0, s29
	s_nop 0
	buffer_load_dwordx4 v166, s[12:15], s61 offen lds
	v_mfma_f32_16x16x32_bf16 v[132:135], v[68:71], v[148:151], v[132:135]
	ds_read_b128 v[144:147], v169 offset:38912
	s_waitcnt lgkmcnt(4)
	v_mfma_f32_16x16x32_bf16 v[136:139], v[72:75], v[152:155], v[136:139]
	v_mfma_f32_16x16x32_bf16 v[128:131], v[76:79], v[152:155], v[128:131]
	ds_read_b128 v[148:151], v169 offset:39168
	v_and_or_b32 v237, v208, s49, v234
	v_and_or_b32 v238, v216, s49, v235
	v_max_f32_e32 v161, v237, v238
	s_waitcnt lgkmcnt(4)
	v_mfma_f32_16x16x32_bf16 v[140:143], v[72:75], v[156:159], v[140:143]
	v_mfma_f32_16x16x32_bf16 v[132:135], v[76:79], v[156:159], v[132:135]
	ds_read_b128 v[152:155], v169 offset:40960
	v_and_or_b32 v237, v209, s49, v234
	v_and_or_b32 v238, v217, s49, v235
	v_max_f32_e32 v160, v237, v238
	s_waitcnt lgkmcnt(4)
	v_mfma_f32_16x16x32_bf16 v[136:139], v[80:83], v[224:227], v[136:139]
	v_mfma_f32_16x16x32_bf16 v[128:131], v[84:87], v[224:227], v[128:131]
	ds_read_b128 v[156:159], v169 offset:41216
	v_and_or_b32 v237, v210, s49, v234
	v_and_or_b32 v238, v218, s49, v235
	v_max_f32_e32 v162, v237, v238
	s_waitcnt lgkmcnt(4)
	v_mfma_f32_16x16x32_bf16 v[140:143], v[80:83], v[228:231], v[140:143]
	s_or_b32 s61, s60, 0x6000
	s_mov_b32 m0, s30
	s_nop 0
	buffer_load_dwordx4 v166, s[12:15], s61 offen lds
	v_mfma_f32_16x16x32_bf16 v[132:135], v[84:87], v[228:231], v[132:135]
	ds_read_b128 v[224:227], v169 offset:43008
	v_and_or_b32 v237, v211, s49, v234
	v_and_or_b32 v238, v219, s49, v235
	v_max_f32_e32 v163, v237, v238
	s_waitcnt lgkmcnt(4)
	v_mfma_f32_16x16x32_bf16 v[136:139], v[88:91], v[144:147], v[136:139]
	v_mfma_f32_16x16x32_bf16 v[128:131], v[92:95], v[144:147], v[128:131]
	ds_read_b128 v[228:231], v169 offset:43264
	v_and_or_b32 v237, v212, s49, v234
	v_and_or_b32 v238, v220, s49, v235
	v_max_f32_e32 v203, v237, v238
	s_waitcnt lgkmcnt(4)
	v_mfma_f32_16x16x32_bf16 v[140:143], v[88:91], v[148:151], v[140:143]
	v_mfma_f32_16x16x32_bf16 v[132:135], v[92:95], v[148:151], v[132:135]
	ds_read_b128 v[144:147], v169 offset:45056
	v_and_or_b32 v237, v213, s49, v234
	v_and_or_b32 v238, v221, s49, v235
	v_max_f32_e32 v204, v237, v238
	s_waitcnt lgkmcnt(4)
	v_mfma_f32_16x16x32_bf16 v[136:139], v[96:99], v[152:155], v[136:139]
	v_mfma_f32_16x16x32_bf16 v[128:131], v[100:103], v[152:155], v[128:131]
	ds_read_b128 v[148:151], v169 offset:45312
	v_and_or_b32 v237, v214, s49, v234
	v_and_or_b32 v238, v222, s49, v235
	v_max_f32_e32 v205, v237, v238
	s_waitcnt lgkmcnt(4)
	v_mfma_f32_16x16x32_bf16 v[140:143], v[96:99], v[156:159], v[140:143]
	s_or_b32 s61, s60, 0xc000
	s_mov_b32 m0, s31
	s_nop 0
	buffer_load_dwordx4 v166, s[12:15], s61 offen lds
	v_mfma_f32_16x16x32_bf16 v[132:135], v[100:103], v[156:159], v[132:135]
	ds_read_b128 v[152:155], v169 offset:47104
	v_and_or_b32 v237, v215, s49, v234
	v_and_or_b32 v238, v223, s49, v235
	v_max_f32_e32 v206, v237, v238
	s_waitcnt lgkmcnt(4)
	v_mfma_f32_16x16x32_bf16 v[136:139], v[104:107], v[224:227], v[136:139]
	v_mfma_f32_16x16x32_bf16 v[128:131], v[108:111], v[224:227], v[128:131]
	ds_read_b128 v[156:159], v169 offset:47360
	s_waitcnt lgkmcnt(4)
	v_mfma_f32_16x16x32_bf16 v[140:143], v[104:107], v[228:231], v[140:143]
	v_mfma_f32_16x16x32_bf16 v[132:135], v[108:111], v[228:231], v[132:135]
	s_waitcnt lgkmcnt(3)
	v_mfma_f32_16x16x32_bf16 v[136:139], v[112:115], v[144:147], v[136:139]
	v_mfma_f32_16x16x32_bf16 v[128:131], v[116:119], v[144:147], v[128:131]
	s_waitcnt lgkmcnt(2)
	v_mfma_f32_16x16x32_bf16 v[140:143], v[112:115], v[148:151], v[140:143]
	s_or_b32 s61, s60, 0xe000
	s_mov_b32 m0, s33
	s_nop 0
	buffer_load_dwordx4 v166, s[12:15], s61 offen lds
	v_mfma_f32_16x16x32_bf16 v[132:135], v[116:119], v[148:151], v[132:135]
	s_waitcnt lgkmcnt(1)
	v_mfma_f32_16x16x32_bf16 v[136:139], v[120:123], v[152:155], v[136:139]
	v_mfma_f32_16x16x32_bf16 v[128:131], v[124:127], v[152:155], v[128:131]
	s_waitcnt lgkmcnt(0)
	v_mfma_f32_16x16x32_bf16 v[140:143], v[120:123], v[156:159], v[140:143]
	v_mfma_f32_16x16x32_bf16 v[132:135], v[124:127], v[156:159], v[132:135]
	v_lshl_or_b32 v202, v167, 2, s47
	v_add_u32_e32 v202, 0x1ff00, v202
	s_add_i32 s50, s50, -4
	s_mov_b32 s51, -1.0
	s_movk_i32 s52, 0xff80
	s_brev_b32 s53, -2
	ds_read_b128 v[144:147], v168
	ds_read_b128 v[148:151], v168 offset:256
	ds_read_b128 v[152:155], v168 offset:2048
	ds_read_b128 v[156:159], v168 offset:2304
	s_waitcnt vmcnt(0)
	s_branch .LBB3_13
